# MLA key loops: lead half issues QK MFMAs before its LDS reads and DMA, lag half issues reads and DMA before softmax; dead m0 saves removed
# speedup vs baseline: 1.0024x; 1.0024x over previous
; #define ATT_SB() __builtin_amdgcn_sched_barrier(0)
; #define ATT_DMA_K(t, sl) do { glds16(ksrc + (size_t)(t) * 64 * kpitch, (unsigned)__builtin_amdgcn_readfirstlane(kdst + (sl) * KSLOT)); \
;         if constexpr (DQK == 96) glds16(krsrc + (size_t)(t) * 64 * 32, (unsigned)__builtin_amdgcn_readfirstlane(krdst + (sl) * KSLOT)); } while (0)
; #define ATT_DMA_V(t, sl) do { glds16(vsrc + (size_t)(t) * 64, (unsigned)__builtin_amdgcn_readfirstlane(vdst + (sl) * VSLOT)); \
;         if constexpr (DV == 128) glds16(vsrc + (size_t)64 * NR + (size_t)(t) * 64, (unsigned)__builtin_amdgcn_readfirstlane(vdst + (sl) * VSLOT + 8192)); } while (0)
; template <int DQK, int DV, bool LEAD> ...
;     ...
;     for (int t = 1; t < NT; ++t) {
;         __builtin_amdgcn_s_waitcnt(0xC07F);
;         if constexpr (!LEAD) { ATT_EXP(); ATT_SUMPACK(); ATT_SB(); }
;         ATT_VLOAD(s_prev, 0); ATT_SB();
;         { const int tk = (t + 3 < NT) ? t + 3 : NT - 1; ATT_DMA_K(tk, s_cur); }
;         { const int tv = (t + 1 < NT) ? t + 1 : NT - 1; ATT_DMA_V(tv, s_next); }
;         ATT_SB();
;         if constexpr (LEAD) {
;             ATT_QK(); ATT_SB();
;             ATT_PVP(0); ATT_SB();
;             if constexpr (DV == 128) { ATT_VLOAD(s_prev, 1); ATT_SB(); ATT_EXP(); ATT_SB(); ATT_PVP(1); ATT_SB(); }
;             if (one_) ATT_KLOAD(s_next);
;             ATT_SB();
;             if constexpr (DV == 64) ATT_EXP();
;             ATT_SUMPACK();
;             asm volatile("" : "+v"(pw[0]), "+v"(pw[1]), "+v"(pw[2]), "+v"(pw[3]));
; #pragma unroll
;             for (int qb = 0; qb < NQB; ++qb) asm volatile("" : "+v"(lsum[qb]));
;         } else {
;             if constexpr (DV == 128) {
;                 ATT_PVP(0); ATT_SB();
;                 ATT_VLOAD(s_prev, 1); ATT_SB();
;                 ATT_QK(); ATT_SB();
;                 if (one_) { ATT_KLOAD(s_next); ATT_SB(); ATT_PVP(1); }
;                 ATT_SB();
;             } else {
;                 __builtin_amdgcn_s_setprio(1);
;                 ATT_QK(); ATT_SB();
;                 if (one_) { ATT_KLOAD(s_next); ATT_SB(); ATT_PVP(0); }
;                 ATT_SB();
;                 __builtin_amdgcn_s_setprio(0);
;             }
.LBB0_643:
	s_mov_b32 s5, s16
	s_mov_b32 s16, s38
	s_add_i32 s38, s48, -1
	v_lshl_add_u32 v70, s4, 13, v210
	ds_read_b128 v[188:191], v70 offset:36864
	ds_read_b128 v[184:187], v70 offset:38912
	ds_read_b128 v[180:183], v70 offset:40960
	ds_read_b128 v[176:179], v70 offset:43008
	s_min_u32 s38, s38, 0x80
	s_add_i32 s49, s38, 3
	s_lshl_b32 s38, s49, 17
	s_mul_i32 s54, s5, 0x3000
	v_lshl_add_u64 v[208:209], v[192:193], 0, s[38:39]
	s_add_i32 s38, s54, s42
	s_mov_b32 m0, s38
	s_nop 0
	global_load_lds_dwordx4 v[208:209], off
	s_lshl_b32 s38, s49, 12
	v_lshl_add_u64 v[208:209], v[204:205], 0, s[38:39]
	s_add_i32 s38, s54, s43
	s_mov_b32 m0, s38
	s_nop 0
	global_load_lds_dwordx4 v[208:209], off
	s_min_u32 s38, s48, 0x83
	s_lshl_b32 s38, s38, 7
	v_lshl_add_u64 v[208:209], v[206:207], 0, s[38:39]
	s_lshl_b32 s38, s16, 13
	s_add_i32 s38, s38, s41
	s_mov_b32 m0, s38
	s_nop 0
	global_load_lds_dwordx4 v[208:209], off
	v_exp_f32_e32 v213, v164
	v_exp_f32_e32 v214, v165
	v_exp_f32_e32 v215, v166
	v_exp_f32_e32 v216, v167
	v_exp_f32_e32 v217, v152
	v_exp_f32_e32 v218, v153
	v_exp_f32_e32 v219, v154
	v_exp_f32_e32 v220, v155
	v_exp_f32_e32 v221, v144
	v_exp_f32_e32 v236, v145
	v_exp_f32_e32 v238, v146
	v_exp_f32_e32 v240, v147
	v_exp_f32_e32 v243, v136
	v_exp_f32_e32 v244, v137
	v_exp_f32_e32 v246, v138
	v_exp_f32_e32 v248, v139
	v_add_f32_e32 v70, v213, v214
	v_add_f32_e32 v71, v215, v216
	v_exp_f32_e32 v237, v172
	v_exp_f32_e32 v245, v168
	v_exp_f32_e32 v251, v160
	v_exp_f32_e32 v235, v156
	v_add_f32_e32 v70, v70, v71
	v_add_f32_e32 v71, v217, v218
	v_add_f32_e32 v136, v219, v220
	v_add_f32_e32 v71, v71, v136
	v_add_f32_e32 v136, v221, v236
	v_add_f32_e32 v137, v238, v240
	v_exp_f32_e32 v239, v173
	v_exp_f32_e32 v247, v169
	v_exp_f32_e32 v252, v161
	v_exp_f32_e32 v223, v157
	v_add_f32_e32 v136, v136, v137
	v_add_f32_e32 v137, v243, v244
	v_add_f32_e32 v138, v246, v248
	v_add_f32_e32 v137, v137, v138
	v_exp_f32_e32 v241, v174
	v_exp_f32_e32 v249, v170
	v_exp_f32_e32 v253, v162
	v_exp_f32_e32 v197, v158
	v_add_f32_e32 v70, v237, v70
	v_add_f32_e32 v71, v245, v71
	v_add_f32_e32 v136, v251, v136
	v_add_f32_e32 v137, v235, v137
	s_waitcnt lgkmcnt(0)
	v_exp_f32_e32 v242, v175
	v_exp_f32_e32 v250, v171
	v_exp_f32_e32 v254, v163
	v_exp_f32_e32 v232, v159
	v_add_f32_e32 v70, v239, v70
	v_add_f32_e32 v71, v247, v71
	v_add_f32_e32 v136, v252, v136
	v_add_f32_e32 v137, v223, v137
	v_add_f32_e32 v70, v241, v70
	v_add_f32_e32 v71, v249, v71
	v_add_f32_e32 v136, v253, v136
	v_add_f32_e32 v137, v197, v137
	v_add_f32_e32 v209, v242, v70
	v_add_f32_e32 v208, v250, v71
	v_add_f32_e32 v71, v254, v136
	v_add_f32_e32 v70, v232, v137
	s_setprio 1
	v_mfma_f32_16x16x32_bf16 v[136:139], v[120:123], v[6:9], 0
	v_mfma_f32_16x16x32_bf16 v[144:147], v[120:123], v[26:29], 0
	v_mfma_f32_16x16x32_bf16 v[152:155], v[120:123], v[72:75], 0
	v_mfma_f32_16x16x32_bf16 v[156:159], v[120:123], v[38:41], 0
	v_mfma_f32_16x16x32_bf16 v[136:139], v[124:127], v[2:5], v[136:139]
	v_mfma_f32_16x16x32_bf16 v[144:147], v[124:127], v[16:19], v[144:147]
	v_mfma_f32_16x16x32_bf16 v[160:163], v[124:127], v[58:61], v[152:155]
	v_mfma_f32_16x16x32_bf16 v[156:159], v[124:127], v[42:45], v[156:159]
	v_mfma_f32_16x16x32_bf16 v[164:167], v[128:131], v[10:13], v[136:139]
	v_mfma_f32_16x16x32_bf16 v[152:155], v[128:131], v[34:37], v[144:147]
	v_mfma_f32_16x16x32_bf16 v[144:147], v[128:131], v[46:49], v[160:163]
	v_mfma_f32_16x16x32_bf16 v[136:139], v[128:131], v[54:57], v[156:159]
	v_mfma_f32_16x16x32_bf16 v[156:159], v[132:135], v[6:9], 0
	v_mfma_f32_16x16x32_bf16 v[160:163], v[132:135], v[26:29], 0
	v_mfma_f32_16x16x32_bf16 v[168:171], v[132:135], v[72:75], 0
	v_mfma_f32_16x16x32_bf16 v[172:175], v[132:135], v[38:41], 0
	v_mfma_f32_16x16x32_bf16 v[156:159], v[140:143], v[2:5], v[156:159]
	v_mfma_f32_16x16x32_bf16 v[160:163], v[140:143], v[16:19], v[160:163]
	v_mfma_f32_16x16x32_bf16 v[198:201], v[140:143], v[58:61], v[168:171]
	v_mfma_f32_16x16x32_bf16 v[228:231], v[140:143], v[42:45], v[172:175]
	v_mfma_f32_16x16x32_bf16 v[172:175], v[148:151], v[10:13], v[156:159]
	v_mfma_f32_16x16x32_bf16 v[168:171], v[148:151], v[34:37], v[160:163]
	v_mfma_f32_16x16x32_bf16 v[160:163], v[148:151], v[46:49], v[198:201]
	v_mfma_f32_16x16x32_bf16 v[156:159], v[148:151], v[54:57], v[228:231]
	s_andn2_b64 vcc, exec, s[6:7]
	s_cbranch_vccnz .LBB0_645
	s_mul_i32 s38, s16, 0x3000
	v_add_u32_e32 v148, s38, v212
	v_add_u32_e32 v132, s38, v203
	v_add_u32_e32 v140, s38, v211
	ds_read_b128 v[120:123], v132
	ds_read_b128 v[124:127], v140
	ds_read_b128 v[128:131], v148 offset:8192
	ds_read_b128 v[132:135], v132 offset:512
	ds_read_b128 v[140:143], v140 offset:512
	ds_read_b128 v[148:151], v148 offset:8448
	v_cvt_pk_bf16_f32 v201, v197, v232
	v_cvt_pk_bf16_f32 v200, v235, v223
	v_cvt_pk_bf16_f32 v199, v246, v248
	v_cvt_pk_bf16_f32 v198, v243, v244
	v_cvt_pk_bf16_f32 v231, v253, v254
	v_cvt_pk_bf16_f32 v230, v251, v252
	v_cvt_pk_bf16_f32 v229, v238, v240
	v_cvt_pk_bf16_f32 v228, v221, v236
	v_cvt_pk_bf16_f32 v223, v249, v250
	v_cvt_pk_bf16_f32 v222, v245, v247
	v_cvt_pk_bf16_f32 v221, v219, v220
	v_cvt_pk_bf16_f32 v220, v217, v218
	v_cvt_pk_bf16_f32 v219, v241, v242
	v_cvt_pk_bf16_f32 v218, v237, v239
	v_cvt_pk_bf16_f32 v217, v215, v216
	v_cvt_pk_bf16_f32 v216, v213, v214
	s_waitcnt lgkmcnt(9)
	s_nop 0
	v_mfma_f32_16x16x32_bf16 v[116:119], v[188:191], v[216:219], v[116:119]
	v_mfma_f32_16x16x32_bf16 v[112:115], v[188:191], v[220:223], v[112:115]
	v_mfma_f32_16x16x32_bf16 v[108:111], v[188:191], v[228:231], v[108:111]
	v_mfma_f32_16x16x32_bf16 v[104:107], v[188:191], v[198:201], v[104:107]
	s_waitcnt lgkmcnt(8)
	v_mfma_f32_16x16x32_bf16 v[100:103], v[184:187], v[216:219], v[100:103]
	v_mfma_f32_16x16x32_bf16 v[96:99], v[184:187], v[220:223], v[96:99]
	v_mfma_f32_16x16x32_bf16 v[92:95], v[184:187], v[228:231], v[92:95]
	v_mfma_f32_16x16x32_bf16 v[88:91], v[184:187], v[198:201], v[88:91]
	s_waitcnt lgkmcnt(7)
	v_mfma_f32_16x16x32_bf16 v[84:87], v[180:183], v[216:219], v[84:87]
	v_mfma_f32_16x16x32_bf16 v[80:83], v[180:183], v[220:223], v[80:83]
	v_mfma_f32_16x16x32_bf16 v[76:79], v[180:183], v[228:231], v[76:79]
	v_mfma_f32_16x16x32_bf16 v[66:69], v[180:183], v[198:201], v[66:69]
	s_waitcnt lgkmcnt(6)
	v_mfma_f32_16x16x32_bf16 v[62:65], v[176:179], v[216:219], v[62:65]
	v_mfma_f32_16x16x32_bf16 v[50:53], v[176:179], v[220:223], v[50:53]
	v_mfma_f32_16x16x32_bf16 v[30:33], v[176:179], v[228:231], v[30:33]
	v_mfma_f32_16x16x32_bf16 v[20:23], v[176:179], v[198:201], v[20:23]

; #define ATT_SB() __builtin_amdgcn_sched_barrier(0)
; #define ATT_DMA_K(t, sl) do { glds16(ksrc + (size_t)(t) * 64 * kpitch, (unsigned)__builtin_amdgcn_readfirstlane(kdst + (sl) * KSLOT)); \
;         if constexpr (DQK == 96) glds16(krsrc + (size_t)(t) * 64 * 32, (unsigned)__builtin_amdgcn_readfirstlane(krdst + (sl) * KSLOT)); } while (0)
; #define ATT_DMA_V(t, sl) do { glds16(vsrc + (size_t)(t) * 64, (unsigned)__builtin_amdgcn_readfirstlane(vdst + (sl) * VSLOT)); \
;         if constexpr (DV == 128) glds16(vsrc + (size_t)64 * NR + (size_t)(t) * 64, (unsigned)__builtin_amdgcn_readfirstlane(vdst + (sl) * VSLOT + 8192)); } while (0)
; #define ATT_KLOAD(sl) do { _Pragma("unroll") for (int kb_ = 0; kb_ < NKW; ++kb_) _Pragma("unroll") for (int ds_ = 0; ds_ < NDS; ++ds_) { \
;         if (ds_ < 2) kf[kb_ * NDS + ds_] = *(const LAS bf16x8*)(kp[ds_ & 1] + (sl) * KSLOT + (kb_ & 1) * 512 + (kb_ >> 1) * 4096); \
;         else kf[kb_ * NDS + ds_] = *(const LAS bf16x8*)(krp + (sl) * KSLOT + (kb_ & 1) * 256 + (kb_ >> 1) * 2048); } } while (0)
; #define ATT_QK() do { _Pragma("unroll") for (int kb_ = 0; kb_ < NKW; ++kb_) _Pragma("unroll") for (int ds_ = 0; ds_ < NDS; ++ds_) _Pragma("unroll") for (int qb_ = 0; qb_ < NQB; ++qb_) \
;         c[kb_][qb_] = __builtin_amdgcn_mfma_f32_16x16x32_bf16(kf[kb_ * NDS + ds_], qf[qb_ * NDS + ds_], ds_ == 0 ? zero4 : c[kb_][qb_], 0, 0, 0); } while (0)
; template <int DQK, int DV, bool LEAD> ...
;     ...
;         ATT_VLOAD(s_prev, 0); ATT_SB();
;         { const int tk = (t + 3 < NT) ? t + 3 : NT - 1; ATT_DMA_K(tk, s_cur); }
;         { const int tv = (t + 1 < NT) ? t + 1 : NT - 1; ATT_DMA_V(tv, s_next); }
;         ATT_SB();
;         if constexpr (LEAD) {
;             ATT_QK(); ATT_SB();
;             ATT_PVP(0); ATT_SB();
;             if constexpr (DV == 128) { ATT_VLOAD(s_prev, 1); ATT_SB(); ATT_EXP(); ATT_SB(); ATT_PVP(1); ATT_SB(); }
;             if (one_) ATT_KLOAD(s_next);
;             ATT_SB();
;             if constexpr (DV == 64) ATT_EXP();
;             ATT_SUMPACK();
;             asm volatile("" : "+v"(pw[0]), "+v"(pw[1]), "+v"(pw[2]), "+v"(pw[3]));
; #pragma unroll
;             for (int qb = 0; qb < NQB; ++qb) asm volatile("" : "+v"(lsum[qb]));
.LBB0_650:
	v_mfma_f32_16x16x32_bf16 v[154:157], v[42:45], v[6:9], 0
	v_mfma_f32_16x16x32_bf16 v[158:161], v[42:45], v[18:21], 0
	v_mfma_f32_16x16x32_bf16 v[162:165], v[42:45], v[30:33], 0
	v_mfma_f32_16x16x32_bf16 v[166:169], v[42:45], v[54:57], 0
	v_mfma_f32_16x16x32_bf16 v[154:157], v[50:53], v[2:5], v[154:157]
	v_mfma_f32_16x16x32_bf16 v[158:161], v[50:53], v[14:17], v[158:161]
	v_mfma_f32_16x16x32_bf16 v[162:165], v[50:53], v[26:29], v[162:165]
	v_mfma_f32_16x16x32_bf16 v[166:169], v[50:53], v[58:61], v[166:169]
	v_mfma_f32_16x16x32_bf16 v[182:185], v[66:69], v[10:13], v[154:157]
	v_mfma_f32_16x16x32_bf16 v[178:181], v[66:69], v[22:25], v[158:161]
	v_mfma_f32_16x16x32_bf16 v[170:173], v[66:69], v[34:37], v[162:165]
	v_mfma_f32_16x16x32_bf16 v[162:165], v[66:69], v[38:41], v[166:169]
	v_mfma_f32_16x16x32_bf16 v[154:157], v[46:49], v[6:9], 0
	v_mfma_f32_16x16x32_bf16 v[158:161], v[46:49], v[18:21], 0
	v_mfma_f32_16x16x32_bf16 v[166:169], v[46:49], v[30:33], 0
	v_mfma_f32_16x16x32_bf16 v[174:177], v[46:49], v[54:57], 0
	v_mfma_f32_16x16x32_bf16 v[154:157], v[62:65], v[2:5], v[154:157]
	v_mfma_f32_16x16x32_bf16 v[158:161], v[62:65], v[14:17], v[158:161]
	v_mfma_f32_16x16x32_bf16 v[248:251], v[62:65], v[26:29], v[166:169]
	v_mfma_f32_16x16x32_bf16 v[220:223], v[62:65], v[58:61], v[174:177]
	v_mfma_f32_16x16x32_bf16 v[174:177], v[70:73], v[10:13], v[154:157]
	v_mfma_f32_16x16x32_bf16 v[166:169], v[70:73], v[22:25], v[158:161]
	v_mfma_f32_16x16x32_bf16 v[158:161], v[70:73], v[34:37], v[248:251]
	v_mfma_f32_16x16x32_bf16 v[154:157], v[70:73], v[38:41], v[220:223]
	v_lshl_add_u32 v252, s24, 13, v210
	ds_read_b128 v[212:215], v252 offset:36864
	ds_read_b128 v[236:239], v252 offset:38912
	ds_read_b128 v[240:243], v252 offset:40960
	ds_read_b128 v[244:247], v252 offset:43008
	s_mov_b32 s31, s16
	s_mov_b32 s16, s38
	s_add_i32 s38, s7, -1
	s_min_u32 s38, s38, 0x80
	s_add_i32 s43, s38, 3
	s_lshl_b32 s38, s43, 17
	s_mul_i32 s44, s31, 0x3000
	v_lshl_add_u64 v[252:253], v[186:187], 0, s[38:39]
	s_add_i32 s38, s44, s42
	s_mov_b32 m0, s38
	s_nop 0
	global_load_lds_dwordx4 v[252:253], off
	s_lshl_b32 s38, s43, 12
	v_lshl_add_u64 v[252:253], v[188:189], 0, s[38:39]
	s_add_i32 s38, s44, s41
	s_mov_b32 m0, s38
	s_nop 0
	global_load_lds_dwordx4 v[252:253], off
	s_min_u32 s38, s7, 0x83
	s_lshl_b32 s38, s38, 7
	v_lshl_add_u64 v[252:253], v[190:191], 0, s[38:39]
	s_lshl_b32 s38, s16, 13
	s_add_i32 s38, s38, s40
	s_mov_b32 m0, s38
	s_nop 0
	global_load_lds_dwordx4 v[252:253], off
	s_waitcnt lgkmcnt(3)
	v_mfma_f32_16x16x32_bf16 v[134:137], v[212:215], v[138:141], v[134:137]
	v_mfma_f32_16x16x32_bf16 v[130:133], v[212:215], v[142:145], v[130:133]
	v_mfma_f32_16x16x32_bf16 v[126:129], v[212:215], v[146:149], v[126:129]
	v_mfma_f32_16x16x32_bf16 v[122:125], v[212:215], v[150:153], v[122:125]
	s_waitcnt lgkmcnt(2)
	v_mfma_f32_16x16x32_bf16 v[118:121], v[236:239], v[138:141], v[118:121]
	v_mfma_f32_16x16x32_bf16 v[114:117], v[236:239], v[142:145], v[114:117]
	v_mfma_f32_16x16x32_bf16 v[110:113], v[236:239], v[146:149], v[110:113]
	v_mfma_f32_16x16x32_bf16 v[106:109], v[236:239], v[150:153], v[106:109]
	s_waitcnt lgkmcnt(1)
	v_mfma_f32_16x16x32_bf16 v[102:105], v[240:243], v[138:141], v[102:105]
	v_mfma_f32_16x16x32_bf16 v[98:101], v[240:243], v[142:145], v[98:101]
	v_mfma_f32_16x16x32_bf16 v[94:97], v[240:243], v[146:149], v[94:97]
	v_mfma_f32_16x16x32_bf16 v[90:93], v[240:243], v[150:153], v[90:93]
	s_waitcnt lgkmcnt(0)
	v_mfma_f32_16x16x32_bf16 v[86:89], v[244:247], v[138:141], v[86:89]
	v_mfma_f32_16x16x32_bf16 v[82:85], v[244:247], v[142:145], v[82:85]
	v_mfma_f32_16x16x32_bf16 v[78:81], v[244:247], v[146:149], v[78:81]
	v_mfma_f32_16x16x32_bf16 v[74:77], v[244:247], v[150:153], v[74:77]
	s_andn2_b64 vcc, exec, s[4:5]
	s_cbranch_vccnz .LBB0_652
	s_mul_i32 s38, s16, 0x3000
	v_add_u32_e32 v70, s38, v209
	v_add_u32_e32 v46, s38, v219
	v_add_u32_e32 v62, s38, v208
	ds_read_b128 v[42:45], v46
	ds_read_b128 v[46:49], v46 offset:512
	ds_read_b128 v[50:53], v62
	ds_read_b128 v[62:65], v62 offset:512
	ds_read_b128 v[66:69], v70 offset:8192
	ds_read_b128 v[70:73], v70 offset:8448
